# weight-conversion part D moved into FFN1 epilogues, dwordx4 loads: 4 tiles every other unit, each wave one 32x64 half tile, loads in flight across the SwiGLU epilogue
# speedup vs baseline: 1.0048x; 1.0048x over previous
.LBB0_1908:
	v_readlane_b32 s78, v254, 2
	v_readlane_b32 s79, v254, 3
	v_readlane_b32 s72, v254, 10
	v_lshrrev_b32_e32 v2, 6, v0
	s_nop 4
	s_load_dwordx2 s[80:81], s[78:79], 0x100
	s_load_dwordx2 s[78:79], s[78:79], 0x118
	v_readfirstlane_b32 s32, v2
	s_waitcnt lgkmcnt(0)
	s_lshl_b32 s72, s72, 27
	s_add_u32 s80, s80, s72
	s_addc_u32 s81, s81, 0
	s_and_b32 s72, s32, 1
	s_lshl_b32 s72, s72, 17
	s_add_u32 s80, s80, s72
	s_addc_u32 s81, s81, 0
	s_add_u32 s78, s78, 0x9bb0000
	s_addc_u32 s79, s79, 0
	s_and_b32 s72, s32, 1
	s_lshl_b32 s72, s72, 5
	s_add_u32 s78, s78, s72
	s_addc_u32 s79, s79, 0
	s_lshr_b32 s72, s32, 1
	s_lshl_b32 s72, s72, 8
	v_writelane_b32 v255, s80, 40
	v_writelane_b32 v255, s81, 41
	v_writelane_b32 v255, s78, 42
	v_writelane_b32 v255, s79, 43
	v_writelane_b32 v255, s72, 44
	s_mov_b32 s32, 0
	v_readlane_b32 s8, v255, 3
	v_readlane_b32 s9, v255, 4
	s_and_b64 s[8:9], s[8:9], exec
	v_readlane_b32 s0, v254, 2
	s_cselect_b32 s3, 16, 17
	v_readlane_b32 s1, v254, 3
	v_mov_b32_e32 v2, v0
	s_lshl_b32 s8, s3, 8
	s_mov_b32 s6, s2
	s_cmp_ge_i32 s6, s8
	v_readfirstlane_b32 s10, v2
	s_cbranch_scc1 .LBB0_1922
	s_waitcnt vmcnt(0)
	v_ashrrev_i32_e32 v5, 31, v2
	v_lshrrev_b32_e32 v5, 26, v5
	v_add_u32_e32 v5, v2, v5
	v_ashrrev_i32_e32 v12, 6, v5
	v_bfe_i32 v5, v2, 27, 1
	v_lshlrev_b32_e32 v4, 4, v2
	v_lshrrev_b32_e32 v5, 22, v5
	v_add_u32_e32 v5, v4, v5
	v_and_b32_e32 v5, 0xfffffc00, v5
	v_sub_u32_e32 v5, v4, v5
	v_lshrrev_b32_e32 v6, 4, v5
	s_load_dwordx2 s[38:39], s[0:1], 0x118
	v_bitop3_b32 v13, v6, v5, 32 bitop3:0x6c
	v_ashrrev_i32_e32 v5, 31, v5
	v_lshrrev_b32_e32 v5, 26, v5
	v_add_u32_e32 v5, v13, v5
	v_add_u32_e32 v4, 0x2000, v4
	v_ashrrev_i32_e32 v14, 6, v5
	v_ashrrev_i32_e32 v5, 31, v4
	v_lshrrev_b32_e32 v5, 22, v5
	s_waitcnt lgkmcnt(0)
	s_add_u32 s26, s38, 0x163b0000
	v_add_u32_e32 v5, v4, v5
	s_addc_u32 s27, s39, 0
	v_ashrrev_i32_e32 v15, 10, v5
	s_add_u32 s11, s38, 0x1bb0000
	v_mul_i32_i24_e32 v5, 0x400, v15
	s_addc_u32 s12, s39, 0
	v_sub_u32_e32 v4, v4, v5
	s_add_u32 s21, s38, 0x233f0000
	v_lshrrev_b32_e32 v5, 4, v4
	s_addc_u32 s25, s39, 0
	v_bitop3_b32 v16, v5, v4, 32 bitop3:0x6c
	v_lshlrev_b32_e32 v5, 3, v12
	s_lshl_b32 s59, s3, 4
	v_and_b32_e32 v5, -16, v5
	s_abs_i32 s60, s59
	v_add_u32_e32 v6, v14, v5
	v_cvt_f32_u32_e32 v5, s60
	s_ashr_i32 s9, s6, 31
	s_lshr_b32 s9, s9, 29
	s_add_i32 s9, s6, s9
	v_rcp_iflag_f32_e32 v5, v5
	s_ashr_i32 s36, s9, 3
	s_and_b32 s9, s9, -8
	s_sub_i32 s6, s6, s9
	v_mul_f32_e32 v5, 0x4f7ffffe, v5
	v_cvt_u32_f32_e32 v5, v5
	s_lshl_b32 s58, s3, 5
	s_lshr_b32 s9, s6, 31
	s_or_b32 s9, s9, s58
	s_mul_i32 s6, s9, s6
	s_add_i32 s6, s6, s36
	s_sub_i32 s36, 0, s60
	v_readfirstlane_b32 s62, v5
	s_mul_i32 s36, s36, s62
	s_ashr_i32 s9, s6, 31
	s_bfe_i32 s61, s3, 0x1001b
	s_mul_hi_u32 s36, s62, s36
	s_xor_b32 s3, s9, s61
	s_abs_i32 s9, s6
	s_add_i32 s62, s62, s36
	s_mul_hi_u32 s36, s9, s62
	s_mul_i32 s37, s36, s60
	s_ashr_i32 s1, s10, 6
	s_sub_i32 s9, s9, s37
	s_ashr_i32 s0, s10, 8
	s_lshl_b32 s56, s1, 10
	s_add_i32 s37, s36, 1
	s_sub_i32 s40, s9, s60
	s_cmp_ge_u32 s9, s60
	s_cselect_b32 s36, s37, s36
	s_cselect_b32 s9, s40, s9
	s_add_i32 s37, s36, 1
	s_cmp_ge_u32 s9, s60
	s_cselect_b32 s9, s37, s36
	s_xor_b32 s9, s9, s3
	s_sub_i32 s40, s9, s3
	s_mul_i32 s3, s40, s59
	s_sub_i32 s3, s6, s3
	s_bfe_u32 s9, s3, 0x4001b
	s_add_i32 s9, s3, s9
	s_sext_i32_i16 s36, s9
	v_ashrrev_i32_e32 v4, 31, v16
	s_mul_i32 s6, s40, 17
	s_ashr_i32 s36, s36, 4
	v_lshrrev_b32_e32 v4, 26, v4
	s_add_i32 s48, s6, s36
	v_add_u32_e32 v17, v16, v4
	v_lshlrev_b32_e32 v4, 3, v15
	s_and_b32 s6, s9, 0xfff0
	s_ashr_i32 s49, s48, 31
	v_ashrrev_i32_e32 v18, 6, v17
	v_and_b32_e32 v4, -16, v4
	s_sub_i32 s42, s3, s6
	s_lshl_b64 s[36:37], s[48:49], 10
	v_add_u32_e32 v4, v18, v4
	s_add_u32 s36, s21, s36
	s_addc_u32 s37, s25, s37
	v_ashrrev_i32_e32 v7, 31, v6
	v_ashrrev_i32_e32 v5, 31, v4
	v_mov_b32_e32 v117, 0x7a7a7a7a
	v_mov_b32_e32 v198, 0x7f7f7f7f
	v_lshl_add_u64 v[8:9], v[6:7], 2, s[36:37]
	v_lshl_add_u64 v[10:11], v[4:5], 2, s[36:37]
	s_load_dword s57, s[96:97], 0x0
	global_load_dword v19, v[8:9], off
	global_load_dword v20, v[10:11], off
	s_nop 0
	global_load_dword v10, v[10:11], off offset:512
	s_nop 0
	global_load_dword v8, v[8:9], off offset:512
	v_mul_i32_i24_e32 v11, 64, v14
	v_sub_u32_e32 v11, v13, v11
	v_lshlrev_b32_e32 v9, 5, v12
	v_ashrrev_i16_sdwa v11, v250, sext(v11) dst_sel:DWORD dst_unused:UNUSED_PAD src0_sel:DWORD src1_sel:BYTE_0
	v_and_b32_e32 v9, 32, v9
	v_bfe_i32 v11, v11, 0, 16
	v_add_lshl_u32 v199, v9, v11, 1
	v_and_b32_e32 v11, 0xc0, v17
	v_sub_u32_e32 v11, v16, v11
	v_lshlrev_b32_e32 v9, 5, v15
	v_ashrrev_i16_sdwa v11, v250, sext(v11) dst_sel:DWORD dst_unused:UNUSED_PAD src0_sel:DWORD src1_sel:BYTE_0
	v_and_b32_e32 v9, 32, v9
	v_bfe_i32 v11, v11, 0, 16
	v_add_lshl_u32 v200, v9, v11, 1
	v_and_b32_e32 v9, 3, v18
	s_mov_b32 s3, 0x3fffe0
	v_lshrrev_b32_e32 v11, 2, v4
	v_lshlrev_b32_e32 v12, 1, v4
	v_and_or_b32 v9, v4, s3, v9
	v_and_b32_e32 v11, 4, v11
	v_and_b32_e32 v12, 24, v12
	v_or3_b32 v9, v9, v11, v12
	s_ashr_i32 s41, s40, 31
	v_lshl_add_u32 v166, v9, 10, v200
	v_and_b32_e32 v9, 3, v14
	s_lshl_b64 s[40:41], s[40:41], 22
	v_and_or_b32 v9, v6, s3, v9
	s_add_u32 s3, s11, s40
	s_addc_u32 s6, s12, s41
	s_bfe_i64 s[40:41], s[42:43], 0x100000
	v_lshrrev_b32_e32 v11, 2, v6
	v_lshlrev_b32_e32 v12, 1, v6
	s_lshl_b64 s[40:41], s[40:41], 18
	v_and_b32_e32 v11, 4, v11
	v_and_b32_e32 v12, 24, v12
	s_add_u32 s50, s3, s40
	v_or3_b32 v9, v9, v11, v12
	s_addc_u32 s51, s6, s41
	s_add_i32 s49, s56, 0
	v_lshl_add_u32 v168, v9, 10, v199
	s_add_i32 m0, s49, 0x10400
	s_add_i32 s63, s49, 0x400
	global_load_lds_dwordx4 v168, s[50:51]
	s_add_i32 m0, s49, 0x12400
	s_add_i32 s64, s49, 0x2400
	global_load_lds_dwordx4 v166, s[50:51]
	s_mov_b32 m0, s63
	s_add_u32 s40, s50, 0x20000
	s_addc_u32 s41, s51, 0
	s_add_i32 s65, s49, 0x4400
	s_add_i32 s66, s49, 0x6400
	v_mov_b32_e32 v169, v3
	v_mov_b32_e32 v167, v3
	v_mov_b32_e32 v185, v3
	v_mov_b32_e32 v181, v3
	v_lshl_add_u64 v[14:15], s[50:51], 0, v[168:169]
	v_lshl_add_u64 v[12:13], s[50:51], 0, v[166:167]
	s_waitcnt vmcnt(0)
	v_lshl_add_u32 v184, v19, 10, v199
	v_lshl_add_u32 v180, v20, 10, v200
	global_load_lds_dwordx4 v184, s[26:27]
	s_mov_b32 m0, s64
	v_lshl_add_u32 v178, v8, 10, v199
	global_load_lds_dwordx4 v180, s[26:27]
	s_add_i32 m0, s49, 0x14400
	v_lshl_add_u32 v176, v10, 10, v200
	global_load_lds_dwordx4 v168, s[40:41]
	s_add_i32 m0, s49, 0x16400
	v_lshl_add_u64 v[10:11], s[26:27], 0, v[184:185]
	global_load_lds_dwordx4 v166, s[40:41]
	s_mov_b32 m0, s65
	s_cmp_lg_u32 s0, 1
	global_load_lds_dwordx4 v178, s[26:27]
	s_mov_b32 m0, s66
	v_lshl_add_u64 v[8:9], s[26:27], 0, v[180:181]
	global_load_lds_dwordx4 v176, s[26:27]
	s_cbranch_scc1 .LBB0_1911
	s_barrier

.LBB0_1912:
	s_and_b32 s72, s32, 1
	s_cbranch_scc1 .Lcvd_p1_end
	s_cmpk_ge_u32 s32, 14
	s_cbranch_scc1 .Lcvd_p1_end
	v_readlane_b32 s72, v255, 44
	s_lshl_b32 s80, s32, 9
	s_add_i32 s80, s80, s2
	s_nop 0
	s_add_i32 s72, s72, s80
	s_cmpk_ge_i32 s72, 7136
	s_cbranch_scc1 .Lcvd_p1_end
	s_addk_i32 s72, 1056
	v_readlane_b32 s78, v255, 40
	v_readlane_b32 s79, v255, 41
	s_lshr_b32 s80, s72, 4
	s_lshl_b32 s80, s80, 18
	s_and_b32 s81, s72, 15
	s_lshl_b32 s81, s81, 8
	s_add_i32 s80, s80, s81
	v_bfe_u32 v24, v0, 4, 2
	v_lshlrev_b32_e32 v24, 15, v24
	v_and_b32_e32 v210, 15, v0
	v_lshl_add_u32 v24, v210, 4, v24
	v_add_u32_e32 v24, s80, v24
	v_add_u32_e32 v214, 0x1000, v24
	v_add_u32_e32 v218, 0x2000, v24
	v_add_u32_e32 v222, 0x3000, v24
	v_add_u32_e32 v230, 0x4000, v24
	v_add_u32_e32 v234, 0x5000, v24
	v_add_u32_e32 v240, 0x6000, v24
	v_add_u32_e32 v244, 0x7000, v24
	global_load_dwordx4 v[210:213], v24, s[78:79]
	global_load_dwordx4 v[214:217], v214, s[78:79]
	global_load_dwordx4 v[218:221], v218, s[78:79]
	global_load_dwordx4 v[222:225], v222, s[78:79]
	global_load_dwordx4 v[230:233], v230, s[78:79]
	global_load_dwordx4 v[234:237], v234, s[78:79]
	global_load_dwordx4 v[240:243], v240, s[78:79]
	global_load_dwordx4 v[244:247], v244, s[78:79]
.Lcvd_p1_end:
	v_mul_f32_e32 v2, 0xbfb8aa3b, v162
	v_mul_f32_e32 v6, 0xbfb8aa3b, v163
	v_exp_f32_e32 v2, v2
	v_exp_f32_e32 v6, v6
	v_mul_f32_e32 v7, 0xbfb8aa3b, v164
	v_mul_f32_e32 v8, 0xbfb8aa3b, v165
	v_add_f32_e32 v2, 1.0, v2
	v_add_f32_e32 v6, 1.0, v6
	v_exp_f32_e32 v7, v7
	v_exp_f32_e32 v8, v8
	v_mul_f32_e32 v9, 0xbfb8aa3b, v154
	v_mul_f32_e32 v10, 0xbfb8aa3b, v155
	v_rcp_f32_e32 v2, v2
	v_rcp_f32_e32 v6, v6
	v_exp_f32_e32 v9, v9
	v_exp_f32_e32 v10, v10
	v_add_f32_e32 v7, 1.0, v7
	v_add_f32_e32 v8, 1.0, v8
	v_mul_f32_e32 v11, 0xbfb8aa3b, v156
	v_mul_f32_e32 v12, 0xbfb8aa3b, v157
	v_mul_f32_e32 v2, v162, v2
	v_mul_f32_e32 v6, v163, v6
	v_rcp_f32_e32 v7, v7
	v_rcp_f32_e32 v8, v8
	v_add_f32_e32 v9, 1.0, v9
	v_add_f32_e32 v10, 1.0, v10
	v_exp_f32_e32 v11, v11
	v_exp_f32_e32 v12, v12
	v_mul_f32_e32 v2, v2, v158
	v_mul_f32_e32 v6, v6, v159
	v_rcp_f32_e32 v9, v9
	v_rcp_f32_e32 v10, v10
	v_med3_f32 v2, v2, s7, v228
	v_med3_f32 v13, v6, s7, v228
	v_mov_b32_e32 v6, v3
	v_cvt_pk_fp8_f32 v6, v2, v13
	v_mul_f32_e32 v7, v164, v7
	v_mul_f32_e32 v8, v165, v8
	v_add_f32_e32 v11, 1.0, v11
	v_add_f32_e32 v12, 1.0, v12
	v_mul_f32_e32 v7, v7, v160
	v_mul_f32_e32 v8, v8, v161
	v_mul_f32_e32 v9, v154, v9
	v_mul_f32_e32 v10, v155, v10
	v_rcp_f32_e32 v11, v11
	v_rcp_f32_e32 v12, v12
	v_mul_f32_e32 v9, v9, v150
	v_mul_f32_e32 v10, v10, v151
	v_med3_f32 v2, v7, s7, v228
	v_med3_f32 v7, v8, s7, v228
	v_cvt_pk_fp8_f32 v6, v2, v7 op_sel:[0,0,1]
	v_med3_f32 v2, v9, s7, v228
	v_med3_f32 v8, v10, s7, v228
	v_mov_b32_e32 v7, v3
	v_cvt_pk_fp8_f32 v7, v2, v8
	v_lshl_add_u32 v4, s48, 8, v181
	v_mul_f32_e32 v11, v156, v11
	v_mul_f32_e32 v12, v157, v12
	v_ashrrev_i32_e32 v5, 31, v4
	v_mul_f32_e32 v11, v11, v152
	v_mul_f32_e32 v12, v12, v153
	v_lshlrev_b64 v[4:5], 11, v[4:5]
	s_lshl_b32 s0, s3, 7
	v_med3_f32 v2, v11, s7, v228
	v_med3_f32 v8, v12, s7, v228
	v_lshl_add_u64 v[4:5], s[40:41], 0, v[4:5]
	s_ashr_i32 s1, s0, 31
	v_cvt_pk_fp8_f32 v7, v2, v8 op_sel:[0,0,1]
	v_lshl_add_u64 v[4:5], v[4:5], 0, s[0:1]
	v_lshl_add_u64 v[4:5], v[4:5], 0, s[76:77]
	v_lshl_add_u64 v[4:5], v[4:5], 0, v[170:171]
	s_nop 15
	s_nop 15
	global_store_dwordx2 v[4:5], v[6:7], off
	v_mul_f32_e32 v2, 0xbfb8aa3b, v146
	v_mul_f32_e32 v6, 0xbfb8aa3b, v147
	v_exp_f32_e32 v2, v2
	v_exp_f32_e32 v6, v6
	v_mul_f32_e32 v7, 0xbfb8aa3b, v148
	v_mul_f32_e32 v8, 0xbfb8aa3b, v149
	v_add_f32_e32 v2, 1.0, v2
	v_add_f32_e32 v6, 1.0, v6
	v_exp_f32_e32 v7, v7
	v_exp_f32_e32 v8, v8
	v_mul_f32_e32 v9, 0xbfb8aa3b, v138
	v_mul_f32_e32 v10, 0xbfb8aa3b, v139
	v_rcp_f32_e32 v2, v2
	v_rcp_f32_e32 v6, v6
	v_exp_f32_e32 v9, v9
	v_exp_f32_e32 v10, v10
	v_add_f32_e32 v7, 1.0, v7
	v_add_f32_e32 v8, 1.0, v8
	v_mul_f32_e32 v11, 0xbfb8aa3b, v140
	v_mul_f32_e32 v12, 0xbfb8aa3b, v141
	v_mul_f32_e32 v2, v146, v2
	v_mul_f32_e32 v6, v147, v6
	v_rcp_f32_e32 v7, v7
	v_rcp_f32_e32 v8, v8
	v_add_f32_e32 v9, 1.0, v9
	v_add_f32_e32 v10, 1.0, v10
	v_exp_f32_e32 v11, v11
	v_exp_f32_e32 v12, v12
	v_mul_f32_e32 v2, v2, v142
	v_mul_f32_e32 v6, v6, v143
	v_rcp_f32_e32 v9, v9
	v_rcp_f32_e32 v10, v10
	v_med3_f32 v2, v2, s7, v228
	v_med3_f32 v13, v6, s7, v228
	v_mov_b32_e32 v6, v3
	v_cvt_pk_fp8_f32 v6, v2, v13
	v_mul_f32_e32 v7, v148, v7
	v_mul_f32_e32 v8, v149, v8
	v_add_f32_e32 v11, 1.0, v11
	v_add_f32_e32 v12, 1.0, v12
	v_mul_f32_e32 v7, v7, v144
	v_mul_f32_e32 v8, v8, v145
	v_mul_f32_e32 v9, v138, v9
	v_mul_f32_e32 v10, v139, v10
	v_rcp_f32_e32 v11, v11
	v_rcp_f32_e32 v12, v12
	v_mul_f32_e32 v9, v9, v134
	v_mul_f32_e32 v10, v10, v135
	v_med3_f32 v2, v7, s7, v228
	v_med3_f32 v7, v8, s7, v228
	v_cvt_pk_fp8_f32 v6, v2, v7 op_sel:[0,0,1]
	v_med3_f32 v2, v9, s7, v228
	v_med3_f32 v8, v10, s7, v228
	v_mov_b32_e32 v7, v3
	v_cvt_pk_fp8_f32 v7, v2, v8
	v_mul_f32_e32 v11, v140, v11
	v_mul_f32_e32 v12, v141, v12
	v_mul_f32_e32 v11, v11, v136
	v_mul_f32_e32 v12, v12, v137
	v_med3_f32 v2, v11, s7, v228
	v_med3_f32 v8, v12, s7, v228
	v_cvt_pk_fp8_f32 v7, v2, v8 op_sel:[0,0,1]
	v_add_co_u32_e32 v8, vcc, s31, v4
	v_mul_f32_e32 v2, 0xbfb8aa3b, v130
	s_nop 0
	v_addc_co_u32_e32 v9, vcc, 0, v5, vcc
	global_store_dwordx2 v[8:9], v[6:7], off
	v_mul_f32_e32 v6, 0xbfb8aa3b, v131
	v_exp_f32_e32 v2, v2
	v_exp_f32_e32 v6, v6
	v_mul_f32_e32 v7, 0xbfb8aa3b, v132
	v_mul_f32_e32 v8, 0xbfb8aa3b, v133
	v_add_f32_e32 v2, 1.0, v2
	v_add_f32_e32 v6, 1.0, v6
	v_exp_f32_e32 v7, v7
	v_exp_f32_e32 v8, v8
	v_mul_f32_e32 v9, 0xbfb8aa3b, v122
	v_mul_f32_e32 v10, 0xbfb8aa3b, v123
	v_rcp_f32_e32 v2, v2
	v_rcp_f32_e32 v6, v6
	v_exp_f32_e32 v9, v9
	v_exp_f32_e32 v10, v10
	v_add_f32_e32 v7, 1.0, v7
	v_add_f32_e32 v8, 1.0, v8
	v_mul_f32_e32 v11, 0xbfb8aa3b, v124
	v_mul_f32_e32 v12, 0xbfb8aa3b, v125
	v_mul_f32_e32 v2, v130, v2
	v_mul_f32_e32 v6, v131, v6
	v_rcp_f32_e32 v7, v7
	v_rcp_f32_e32 v8, v8
	v_add_f32_e32 v9, 1.0, v9
	v_add_f32_e32 v10, 1.0, v10
	v_exp_f32_e32 v11, v11
	v_exp_f32_e32 v12, v12
	v_mul_f32_e32 v2, v2, v126
	v_mul_f32_e32 v6, v6, v127
	v_rcp_f32_e32 v9, v9
	v_rcp_f32_e32 v10, v10
	v_med3_f32 v2, v2, s7, v228
	v_med3_f32 v13, v6, s7, v228
	v_mov_b32_e32 v6, v3
	v_cvt_pk_fp8_f32 v6, v2, v13
	v_mul_f32_e32 v7, v132, v7
	v_mul_f32_e32 v8, v133, v8
	v_add_f32_e32 v11, 1.0, v11
	v_add_f32_e32 v12, 1.0, v12
	v_mul_f32_e32 v7, v7, v128
	v_mul_f32_e32 v8, v8, v129
	v_mul_f32_e32 v9, v122, v9
	v_mul_f32_e32 v10, v123, v10
	v_rcp_f32_e32 v11, v11
	v_rcp_f32_e32 v12, v12
	v_mul_f32_e32 v9, v9, v118
	v_mul_f32_e32 v10, v10, v119
	v_med3_f32 v2, v7, s7, v228
	v_med3_f32 v7, v8, s7, v228
	v_cvt_pk_fp8_f32 v6, v2, v7 op_sel:[0,0,1]
	v_med3_f32 v2, v9, s7, v228
	v_med3_f32 v8, v10, s7, v228
	v_mov_b32_e32 v7, v3
	v_cvt_pk_fp8_f32 v7, v2, v8
	v_mul_f32_e32 v11, v124, v11
	v_mul_f32_e32 v12, v125, v12
	v_mul_f32_e32 v11, v11, v120
	v_mul_f32_e32 v12, v12, v121
	v_med3_f32 v2, v11, s7, v228
	v_med3_f32 v8, v12, s7, v228
	v_cvt_pk_fp8_f32 v7, v2, v8 op_sel:[0,0,1]
	s_mov_b32 s0, 0x10000
	v_add_co_u32_e32 v8, vcc, s0, v4
	v_mul_f32_e32 v2, 0xbfb8aa3b, v112
	s_nop 0
	v_addc_co_u32_e32 v9, vcc, 0, v5, vcc
	global_store_dwordx2 v[8:9], v[6:7], off
	v_mul_f32_e32 v6, 0xbfb8aa3b, v113
	v_exp_f32_e32 v2, v2
	v_exp_f32_e32 v6, v6
	v_mul_f32_e32 v7, 0xbfb8aa3b, v114
	v_mul_f32_e32 v8, 0xbfb8aa3b, v115
	v_add_f32_e32 v2, 1.0, v2
	v_add_f32_e32 v6, 1.0, v6
	v_exp_f32_e32 v7, v7
	v_exp_f32_e32 v8, v8
	v_mul_f32_e32 v9, 0xbfb8aa3b, v104
	v_mul_f32_e32 v10, 0xbfb8aa3b, v105
	v_rcp_f32_e32 v2, v2
	v_rcp_f32_e32 v6, v6
	v_exp_f32_e32 v9, v9
	v_exp_f32_e32 v10, v10
	v_add_f32_e32 v7, 1.0, v7
	v_add_f32_e32 v8, 1.0, v8
	v_mul_f32_e32 v11, 0xbfb8aa3b, v106
	v_mul_f32_e32 v12, 0xbfb8aa3b, v107
	v_mul_f32_e32 v2, v112, v2
	v_mul_f32_e32 v6, v113, v6
	v_rcp_f32_e32 v7, v7
	v_rcp_f32_e32 v8, v8
	v_add_f32_e32 v9, 1.0, v9
	v_add_f32_e32 v10, 1.0, v10
	v_exp_f32_e32 v11, v11
	v_exp_f32_e32 v12, v12
	v_mul_f32_e32 v2, v2, v108
	v_mul_f32_e32 v6, v6, v109
	v_rcp_f32_e32 v9, v9
	v_rcp_f32_e32 v10, v10
	v_med3_f32 v2, v2, s7, v228
	v_med3_f32 v13, v6, s7, v228
	v_mov_b32_e32 v6, v3
	v_cvt_pk_fp8_f32 v6, v2, v13
	v_mul_f32_e32 v7, v114, v7
	v_mul_f32_e32 v8, v115, v8
	v_add_f32_e32 v11, 1.0, v11
	v_add_f32_e32 v12, 1.0, v12
	v_mul_f32_e32 v7, v7, v110
	v_mul_f32_e32 v8, v8, v111
	v_mul_f32_e32 v9, v104, v9
	v_mul_f32_e32 v10, v105, v10
	v_rcp_f32_e32 v11, v11
	v_rcp_f32_e32 v12, v12
	v_mul_f32_e32 v9, v9, v100
	v_mul_f32_e32 v10, v10, v101
	v_med3_f32 v2, v7, s7, v228
	v_med3_f32 v7, v8, s7, v228
	v_cvt_pk_fp8_f32 v6, v2, v7 op_sel:[0,0,1]
	v_med3_f32 v2, v9, s7, v228
	v_med3_f32 v8, v10, s7, v228
	v_mov_b32_e32 v7, v3
	v_cvt_pk_fp8_f32 v7, v2, v8
	v_mul_f32_e32 v11, v106, v11
	v_mul_f32_e32 v12, v107, v12
	v_mul_f32_e32 v11, v11, v102
	v_mul_f32_e32 v12, v12, v103
	v_med3_f32 v2, v11, s7, v228
	v_med3_f32 v8, v12, s7, v228
	v_cvt_pk_fp8_f32 v7, v2, v8 op_sel:[0,0,1]
	s_mov_b32 s0, 0x18000
	v_add_co_u32_e32 v8, vcc, s0, v4
	v_mul_f32_e32 v2, 0xbfb8aa3b, v96
	s_nop 0
	v_addc_co_u32_e32 v9, vcc, 0, v5, vcc
	global_store_dwordx2 v[8:9], v[6:7], off
	v_mul_f32_e32 v6, 0xbfb8aa3b, v97
	v_exp_f32_e32 v2, v2
	v_exp_f32_e32 v6, v6
	v_mul_f32_e32 v7, 0xbfb8aa3b, v98
	v_mul_f32_e32 v8, 0xbfb8aa3b, v99
	v_add_f32_e32 v2, 1.0, v2
	v_add_f32_e32 v6, 1.0, v6
	v_exp_f32_e32 v7, v7
	v_exp_f32_e32 v8, v8
	v_mul_f32_e32 v9, 0xbfb8aa3b, v88
	v_mul_f32_e32 v10, 0xbfb8aa3b, v89
	v_rcp_f32_e32 v2, v2
	v_rcp_f32_e32 v6, v6
	v_exp_f32_e32 v9, v9
	v_exp_f32_e32 v10, v10
	v_add_f32_e32 v7, 1.0, v7
	v_add_f32_e32 v8, 1.0, v8
	v_mul_f32_e32 v11, 0xbfb8aa3b, v90
	v_mul_f32_e32 v12, 0xbfb8aa3b, v91
	v_mul_f32_e32 v2, v96, v2
	v_mul_f32_e32 v6, v97, v6
	v_rcp_f32_e32 v7, v7
	v_rcp_f32_e32 v8, v8
	v_add_f32_e32 v9, 1.0, v9
	v_add_f32_e32 v10, 1.0, v10
	v_exp_f32_e32 v11, v11
	v_exp_f32_e32 v12, v12
	v_mul_f32_e32 v2, v2, v92
	v_mul_f32_e32 v6, v6, v93
	v_rcp_f32_e32 v9, v9
	v_rcp_f32_e32 v10, v10
	v_med3_f32 v2, v2, s7, v228
	v_med3_f32 v13, v6, s7, v228
	v_mov_b32_e32 v6, v3
	v_cvt_pk_fp8_f32 v6, v2, v13
	v_mul_f32_e32 v7, v98, v7
	v_mul_f32_e32 v8, v99, v8
	v_add_f32_e32 v11, 1.0, v11
	v_add_f32_e32 v12, 1.0, v12
	v_mul_f32_e32 v7, v7, v94
	v_mul_f32_e32 v8, v8, v95
	v_mul_f32_e32 v9, v88, v9
	v_mul_f32_e32 v10, v89, v10
	v_rcp_f32_e32 v11, v11
	v_rcp_f32_e32 v12, v12
	v_mul_f32_e32 v9, v9, v84
	v_mul_f32_e32 v10, v10, v85
	v_med3_f32 v2, v7, s7, v228
	v_med3_f32 v7, v8, s7, v228
	v_cvt_pk_fp8_f32 v6, v2, v7 op_sel:[0,0,1]
	v_med3_f32 v2, v9, s7, v228
	v_med3_f32 v8, v10, s7, v228
	v_mov_b32_e32 v7, v3
	v_cvt_pk_fp8_f32 v7, v2, v8
	v_mul_f32_e32 v11, v90, v11
	v_mul_f32_e32 v12, v91, v12
	v_mul_f32_e32 v11, v11, v86
	v_mul_f32_e32 v12, v12, v87
	v_med3_f32 v2, v11, s7, v228
	v_med3_f32 v8, v12, s7, v228
	v_cvt_pk_fp8_f32 v7, v2, v8 op_sel:[0,0,1]
	v_add_co_u32_e32 v8, vcc, s16, v4
	v_mul_f32_e32 v2, 0xbfb8aa3b, v80
	s_nop 0
	v_addc_co_u32_e32 v9, vcc, 0, v5, vcc
	global_store_dwordx2 v[8:9], v[6:7], off
	v_mul_f32_e32 v6, 0xbfb8aa3b, v81
	v_exp_f32_e32 v2, v2
	v_exp_f32_e32 v6, v6
	v_mul_f32_e32 v7, 0xbfb8aa3b, v82
	v_mul_f32_e32 v8, 0xbfb8aa3b, v83
	v_add_f32_e32 v2, 1.0, v2
	v_add_f32_e32 v6, 1.0, v6
	v_exp_f32_e32 v7, v7
	v_exp_f32_e32 v8, v8
	v_mul_f32_e32 v9, 0xbfb8aa3b, v72
	v_mul_f32_e32 v10, 0xbfb8aa3b, v73
	v_rcp_f32_e32 v2, v2
	v_rcp_f32_e32 v6, v6
	v_exp_f32_e32 v9, v9
	v_exp_f32_e32 v10, v10
	v_add_f32_e32 v7, 1.0, v7
	v_add_f32_e32 v8, 1.0, v8
	v_mul_f32_e32 v11, 0xbfb8aa3b, v74
	v_mul_f32_e32 v12, 0xbfb8aa3b, v75
	v_mul_f32_e32 v2, v80, v2
	v_mul_f32_e32 v6, v81, v6
	v_rcp_f32_e32 v7, v7
	v_rcp_f32_e32 v8, v8
	v_add_f32_e32 v9, 1.0, v9
	v_add_f32_e32 v10, 1.0, v10
	v_exp_f32_e32 v11, v11
	v_exp_f32_e32 v12, v12
	v_mul_f32_e32 v2, v2, v76
	v_mul_f32_e32 v6, v6, v77
	v_rcp_f32_e32 v9, v9
	v_rcp_f32_e32 v10, v10
	v_med3_f32 v2, v2, s7, v228
	v_med3_f32 v13, v6, s7, v228
	v_mov_b32_e32 v6, v3
	v_cvt_pk_fp8_f32 v6, v2, v13
	v_mul_f32_e32 v7, v82, v7
	v_mul_f32_e32 v8, v83, v8
	v_add_f32_e32 v11, 1.0, v11
	v_add_f32_e32 v12, 1.0, v12
	v_mul_f32_e32 v7, v7, v78
	v_mul_f32_e32 v8, v8, v79
	v_mul_f32_e32 v9, v72, v9
	v_mul_f32_e32 v10, v73, v10
	v_rcp_f32_e32 v11, v11
	v_rcp_f32_e32 v12, v12
	v_mul_f32_e32 v9, v9, v68
	v_mul_f32_e32 v10, v10, v69
	v_med3_f32 v2, v7, s7, v228
	v_med3_f32 v7, v8, s7, v228
	v_cvt_pk_fp8_f32 v6, v2, v7 op_sel:[0,0,1]
	v_med3_f32 v2, v9, s7, v228
	v_med3_f32 v8, v10, s7, v228
	v_mov_b32_e32 v7, v3
	v_cvt_pk_fp8_f32 v7, v2, v8
	v_mul_f32_e32 v11, v74, v11
	v_mul_f32_e32 v12, v75, v12
	v_mul_f32_e32 v11, v11, v70
	v_mul_f32_e32 v12, v12, v71
	v_med3_f32 v2, v11, s7, v228
	v_med3_f32 v8, v12, s7, v228
	v_cvt_pk_fp8_f32 v7, v2, v8 op_sel:[0,0,1]
	s_mov_b32 s0, 0x48000
	v_add_co_u32_e32 v8, vcc, s0, v4
	v_mul_f32_e32 v2, 0xbfb8aa3b, v60
	s_nop 0
	v_addc_co_u32_e32 v9, vcc, 0, v5, vcc
	global_store_dwordx2 v[8:9], v[6:7], off
	v_mul_f32_e32 v6, 0xbfb8aa3b, v61
	v_exp_f32_e32 v2, v2
	v_exp_f32_e32 v6, v6
	v_mul_f32_e32 v7, 0xbfb8aa3b, v62
	v_mul_f32_e32 v8, 0xbfb8aa3b, v63
	v_add_f32_e32 v2, 1.0, v2
	v_add_f32_e32 v6, 1.0, v6
	v_exp_f32_e32 v7, v7
	v_exp_f32_e32 v8, v8
	v_mul_f32_e32 v9, 0xbfb8aa3b, v52
	v_mul_f32_e32 v10, 0xbfb8aa3b, v53
	v_rcp_f32_e32 v2, v2
	v_rcp_f32_e32 v6, v6
	v_exp_f32_e32 v9, v9
	v_exp_f32_e32 v10, v10
	v_add_f32_e32 v7, 1.0, v7
	v_add_f32_e32 v8, 1.0, v8
	v_mul_f32_e32 v11, 0xbfb8aa3b, v54
	v_mul_f32_e32 v12, 0xbfb8aa3b, v55
	v_mul_f32_e32 v2, v60, v2
	v_mul_f32_e32 v6, v61, v6
	v_rcp_f32_e32 v7, v7
	v_rcp_f32_e32 v8, v8
	v_add_f32_e32 v9, 1.0, v9
	v_add_f32_e32 v10, 1.0, v10
	v_exp_f32_e32 v11, v11
	v_exp_f32_e32 v12, v12
	v_mul_f32_e32 v2, v2, v64
	v_mul_f32_e32 v6, v6, v65
	v_rcp_f32_e32 v9, v9
	v_rcp_f32_e32 v10, v10
	v_med3_f32 v2, v2, s7, v228
	v_med3_f32 v13, v6, s7, v228
	v_mov_b32_e32 v6, v3
	v_cvt_pk_fp8_f32 v6, v2, v13
	v_mul_f32_e32 v7, v62, v7
	v_mul_f32_e32 v8, v63, v8
	v_add_f32_e32 v11, 1.0, v11
	v_add_f32_e32 v12, 1.0, v12
	v_mul_f32_e32 v7, v7, v66
	v_mul_f32_e32 v8, v8, v67
	v_mul_f32_e32 v9, v52, v9
	v_mul_f32_e32 v10, v53, v10
	v_rcp_f32_e32 v11, v11
	v_rcp_f32_e32 v12, v12
	v_mul_f32_e32 v9, v9, v56
	v_mul_f32_e32 v10, v10, v57
	v_med3_f32 v2, v7, s7, v228
	v_med3_f32 v7, v8, s7, v228
	v_cvt_pk_fp8_f32 v6, v2, v7 op_sel:[0,0,1]
	v_med3_f32 v2, v9, s7, v228
	v_med3_f32 v8, v10, s7, v228
	v_mov_b32_e32 v7, v3
	v_cvt_pk_fp8_f32 v7, v2, v8
	v_mul_f32_e32 v11, v54, v11
	v_mul_f32_e32 v12, v55, v12
	v_mul_f32_e32 v11, v11, v58
	v_mul_f32_e32 v12, v12, v59
	v_med3_f32 v2, v11, s7, v228
	v_med3_f32 v8, v12, s7, v228
	v_cvt_pk_fp8_f32 v7, v2, v8 op_sel:[0,0,1]
	s_mov_b32 s0, 0x50000
	v_add_co_u32_e32 v8, vcc, s0, v4
	v_mul_f32_e32 v2, 0xbfb8aa3b, v44
	s_nop 0
	v_addc_co_u32_e32 v9, vcc, 0, v5, vcc
	global_store_dwordx2 v[8:9], v[6:7], off
	v_mul_f32_e32 v6, 0xbfb8aa3b, v45
	v_exp_f32_e32 v2, v2
	v_exp_f32_e32 v6, v6
	v_mul_f32_e32 v7, 0xbfb8aa3b, v46
	v_mul_f32_e32 v8, 0xbfb8aa3b, v47
	v_add_f32_e32 v2, 1.0, v2
	v_add_f32_e32 v6, 1.0, v6
	v_exp_f32_e32 v7, v7
	v_exp_f32_e32 v8, v8
	v_mul_f32_e32 v9, 0xbfb8aa3b, v36
	v_mul_f32_e32 v10, 0xbfb8aa3b, v37
	v_rcp_f32_e32 v2, v2
	v_rcp_f32_e32 v6, v6
	v_exp_f32_e32 v9, v9
	v_exp_f32_e32 v10, v10
	v_add_f32_e32 v7, 1.0, v7
	v_add_f32_e32 v8, 1.0, v8
	v_mul_f32_e32 v11, 0xbfb8aa3b, v38
	v_mul_f32_e32 v12, 0xbfb8aa3b, v39
	v_mul_f32_e32 v2, v44, v2
	v_mul_f32_e32 v6, v45, v6
	v_rcp_f32_e32 v7, v7
	v_rcp_f32_e32 v8, v8
	v_add_f32_e32 v9, 1.0, v9
	v_add_f32_e32 v10, 1.0, v10
	v_exp_f32_e32 v11, v11
	v_exp_f32_e32 v12, v12
	v_mul_f32_e32 v2, v2, v48
	v_mul_f32_e32 v6, v6, v49
	v_rcp_f32_e32 v9, v9
	v_rcp_f32_e32 v10, v10
	v_med3_f32 v2, v2, s7, v228
	v_med3_f32 v13, v6, s7, v228
	v_mov_b32_e32 v6, v3
	v_cvt_pk_fp8_f32 v6, v2, v13
	v_mul_f32_e32 v7, v46, v7
	v_mul_f32_e32 v8, v47, v8
	v_add_f32_e32 v11, 1.0, v11
	v_add_f32_e32 v12, 1.0, v12
	v_mul_f32_e32 v7, v7, v50
	v_mul_f32_e32 v8, v8, v51
	v_mul_f32_e32 v9, v36, v9
	v_mul_f32_e32 v10, v37, v10
	v_rcp_f32_e32 v11, v11
	v_rcp_f32_e32 v12, v12
	v_mul_f32_e32 v9, v9, v40
	v_mul_f32_e32 v10, v10, v41
	v_med3_f32 v2, v7, s7, v228
	v_med3_f32 v7, v8, s7, v228
	v_cvt_pk_fp8_f32 v6, v2, v7 op_sel:[0,0,1]
	v_med3_f32 v2, v9, s7, v228
	v_med3_f32 v8, v10, s7, v228
	v_mov_b32_e32 v7, v3
	v_cvt_pk_fp8_f32 v7, v2, v8
	v_mul_f32_e32 v11, v38, v11
	v_mul_f32_e32 v12, v39, v12
	v_mul_f32_e32 v11, v11, v42
	v_mul_f32_e32 v12, v12, v43
	v_med3_f32 v2, v11, s7, v228
	v_med3_f32 v8, v12, s7, v228
	v_cvt_pk_fp8_f32 v7, v2, v8 op_sel:[0,0,1]
	v_add_co_u32_e32 v4, vcc, 0x58000, v4
	v_mov_b32_e32 v176, v204
	s_nop 0
	v_addc_co_u32_e32 v5, vcc, 0, v5, vcc
	s_and_b64 vcc, exec, s[38:39]
	v_mov_b32_e32 v178, v205
	v_mov_b32_e32 v180, v203
	v_mov_b32_e32 v184, v202
	s_mov_b32 s3, s44
	s_mov_b32 s48, s42
	s_mov_b64 s[50:51], s[46:47]
	global_store_dwordx2 v[4:5], v[6:7], off
	s_and_b32 s72, s32, 1
	s_cbranch_scc1 .Lcvd_p2_end
	s_cmpk_ge_u32 s32, 14
	s_cbranch_scc1 .Lcvd_p2_end
	v_readlane_b32 s72, v255, 44
	s_lshl_b32 s80, s32, 9
	s_add_i32 s80, s80, s2
	s_nop 0
	s_add_i32 s72, s72, s80
	s_cmpk_ge_i32 s72, 7136
	s_cbranch_scc1 .Lcvd_p2_end
	s_addk_i32 s72, 1056
	v_readlane_b32 s78, v255, 42
	v_readlane_b32 s79, v255, 43
	s_lshr_b32 s80, s72, 9
	s_lshl_b32 s80, s80, 21
	s_and_b32 s81, s72, 15
	s_lshl_b32 s81, s81, 17
	s_add_i32 s80, s80, s81
	s_bfe_u32 s81, s72, 0x50004
	s_lshl_b32 s81, s81, 6
	s_add_i32 s80, s80, s81
	v_and_b32_e32 v22, 15, v0
	v_lshlrev_b32_e32 v22, 13, v22
	v_bfe_u32 v23, v0, 4, 2
	v_lshl_add_u32 v22, v23, 3, v22
	v_add_u32_e32 v22, s80, v22
	v_add_u32_e32 v23, 0x1000, v22
	s_waitcnt vmcnt(8)
	v_mul_f32_e32 v210, 0x42800000, v210
	v_mul_f32_e32 v211, 0x42800000, v211
	v_mul_f32_e32 v212, 0x42800000, v212
	v_mul_f32_e32 v213, 0x42800000, v213
	v_mul_f32_e32 v214, 0x42800000, v214
	v_mul_f32_e32 v215, 0x42800000, v215
	v_mul_f32_e32 v216, 0x42800000, v216
	v_mul_f32_e32 v217, 0x42800000, v217
	v_mul_f32_e32 v218, 0x42800000, v218
	v_mul_f32_e32 v219, 0x42800000, v219
	v_mul_f32_e32 v220, 0x42800000, v220
	v_mul_f32_e32 v221, 0x42800000, v221
	v_mul_f32_e32 v222, 0x42800000, v222
	v_mul_f32_e32 v223, 0x42800000, v223
	v_mul_f32_e32 v224, 0x42800000, v224
	v_mul_f32_e32 v225, 0x42800000, v225
	v_mul_f32_e32 v230, 0x42800000, v230
	v_mul_f32_e32 v231, 0x42800000, v231
	v_mul_f32_e32 v232, 0x42800000, v232
	v_mul_f32_e32 v233, 0x42800000, v233
	v_mul_f32_e32 v234, 0x42800000, v234
	v_mul_f32_e32 v235, 0x42800000, v235
	v_mul_f32_e32 v236, 0x42800000, v236
	v_mul_f32_e32 v237, 0x42800000, v237
	v_mul_f32_e32 v240, 0x42800000, v240
	v_mul_f32_e32 v241, 0x42800000, v241
	v_mul_f32_e32 v242, 0x42800000, v242
	v_mul_f32_e32 v243, 0x42800000, v243
	v_mul_f32_e32 v244, 0x42800000, v244
	v_mul_f32_e32 v245, 0x42800000, v245
	v_mul_f32_e32 v246, 0x42800000, v246
	v_mul_f32_e32 v247, 0x42800000, v247
	v_med3_f32 v210, v210, s7, v228
	v_med3_f32 v211, v211, s7, v228
	v_med3_f32 v212, v212, s7, v228
	v_med3_f32 v213, v213, s7, v228
	v_med3_f32 v214, v214, s7, v228
	v_med3_f32 v215, v215, s7, v228
	v_med3_f32 v216, v216, s7, v228
	v_med3_f32 v217, v217, s7, v228
	v_med3_f32 v218, v218, s7, v228
	v_med3_f32 v219, v219, s7, v228
	v_med3_f32 v220, v220, s7, v228
	v_med3_f32 v221, v221, s7, v228
	v_med3_f32 v222, v222, s7, v228
	v_med3_f32 v223, v223, s7, v228
	v_med3_f32 v224, v224, s7, v228
	v_med3_f32 v225, v225, s7, v228
	v_med3_f32 v230, v230, s7, v228
	v_med3_f32 v231, v231, s7, v228
	v_med3_f32 v232, v232, s7, v228
	v_med3_f32 v233, v233, s7, v228
	v_med3_f32 v234, v234, s7, v228
	v_med3_f32 v235, v235, s7, v228
	v_med3_f32 v236, v236, s7, v228
	v_med3_f32 v237, v237, s7, v228
	v_med3_f32 v240, v240, s7, v228
	v_med3_f32 v241, v241, s7, v228
	v_med3_f32 v242, v242, s7, v228
	v_med3_f32 v243, v243, s7, v228
	v_med3_f32 v244, v244, s7, v228
	v_med3_f32 v245, v245, s7, v228
	v_med3_f32 v246, v246, s7, v228
	v_med3_f32 v247, v247, s7, v228
	v_cvt_pk_fp8_f32 v14, v210, v214
	v_cvt_pk_fp8_f32 v15, v230, v234
	v_cvt_pk_fp8_f32 v16, v211, v215
	v_cvt_pk_fp8_f32 v17, v231, v235
	v_cvt_pk_fp8_f32 v18, v212, v216
	v_cvt_pk_fp8_f32 v19, v232, v236
	v_cvt_pk_fp8_f32 v20, v213, v217
	v_cvt_pk_fp8_f32 v21, v233, v237
	v_cvt_pk_fp8_f32 v14, v218, v222 op_sel:[0,0,1]
	v_cvt_pk_fp8_f32 v15, v240, v244 op_sel:[0,0,1]
	v_cvt_pk_fp8_f32 v16, v219, v223 op_sel:[0,0,1]
	v_cvt_pk_fp8_f32 v17, v241, v245 op_sel:[0,0,1]
	v_cvt_pk_fp8_f32 v18, v220, v224 op_sel:[0,0,1]
	v_cvt_pk_fp8_f32 v19, v242, v246 op_sel:[0,0,1]
	v_cvt_pk_fp8_f32 v20, v221, v225 op_sel:[0,0,1]
	v_cvt_pk_fp8_f32 v21, v243, v247 op_sel:[0,0,1]
	s_nop 1
	global_store_dwordx2 v22, v[14:15], s[78:79]
	global_store_dwordx2 v22, v[16:17], s[78:79] offset:2048
	global_store_dwordx2 v23, v[18:19], s[78:79]
	global_store_dwordx2 v23, v[20:21], s[78:79] offset:2048
.Lcvd_p2_end:
	s_add_i32 s32, s32, 1
	s_cbranch_vccnz .LBB0_1919
